# P14: nt on final output stores and X2 row loads (streaming)
# baseline (speedup 1.0000x reference)
; __global__ void __launch_bounds__(NTHR, 2) fwd(Args args) {
;     ...
;         for (int t = gw; t < T; t += NGW) {
;             size_t so[TOPK]; float gk[TOPK];
; #pragma unroll
;             for (int k = 0; k < TOPK; ++k) { const int e = WSP(int, WS_SELE)[t * TOPK + k], p = WSP(int, WS_SELP)[t * TOPK + k]; gk[k] = WSP(float, WS_SELG)[t * TOPK + k] * Y8_INV;
;                 so[k] = ((size_t)__shfl(pb, e) * 256 + p) * D; }
;             f32x4 v[8]; float s = 0.f;
; #pragma unroll
;             for (int j = 0; j < 8; ++j) { const int cidx = (j * 64 + lane) * 4; f32x4 a = *(const f32x4*)(X2 + (size_t)t * D + cidx);
; #pragma unroll
;                 for (int k = 0; k < TOPK; ++k) { const unsigned y = *(const unsigned*)(YK + so[k] + cidx); const v2f lo = __builtin_amdgcn_cvt_pk_f32_fp8(y, false), hi = __builtin_amdgcn_cvt_pk_f32_fp8(y, true);
;                     a[0] += gk[k] * lo[0]; a[1] += gk[k] * lo[1]; a[2] += gk[k] * hi[0]; a[3] += gk[k] * hi[1]; }
;                 v[j] = a; s += (a[0] * a[0] + a[1] * a[1]) + (a[2] * a[2] + a[3] * a[3]); }
.LBB0_1674:
	s_add_i32 s10, s2, -3
	s_ashr_i32 s11, s10, 31
	v_lshl_add_u64 v[32:33], v[56:57], 0, s[6:7]
	s_lshl_b64 s[10:11], s[10:11], 2
	v_add_co_u32_e32 v120, vcc, s5, v32
	s_add_u32 s20, s12, s10
	v_lshl_add_u64 v[34:35], v[58:59], 0, s[6:7]
	v_lshl_add_u64 v[36:37], v[60:61], 0, s[6:7]
	v_lshl_add_u64 v[38:39], v[62:63], 0, s[6:7]
	v_lshl_add_u64 v[112:113], v[64:65], 0, s[6:7]
	v_addc_co_u32_e32 v121, vcc, 0, v33, vcc
	s_addc_u32 s21, s13, s11
	global_load_dwordx4 v[96:99], v[34:35], off nt
	global_load_dwordx4 v[100:103], v[36:37], off nt
	global_load_dwordx4 v[104:107], v[38:39], off nt
	global_load_dwordx4 v[108:111], v[112:113], off nt
	s_nop 0
	global_load_dwordx4 v[112:115], v[120:121], off nt
	global_load_dwordx4 v[36:39], v[120:121], off offset:1024 nt
	global_load_dwordx4 v[116:119], v[120:121], off offset:2048 nt
	global_load_dwordx4 v[32:35], v[120:121], off offset:3072 nt
	v_lshl_add_u64 v[76:77], v[66:67], 0, s[6:7]
	global_load_dword v121, v94, s[20:21]
	s_add_u32 s20, s14, s10
	s_addc_u32 s21, s15, s11
	s_add_u32 s10, s16, s10
	s_addc_u32 s11, s17, s11
	global_load_dword v120, v94, s[20:21]
	global_load_dword v123, v94, s[10:11]
	s_add_i32 s20, s2, -2
	s_ashr_i32 s21, s20, 31
	s_lshl_b64 s[10:11], s[20:21], 2
	s_add_u32 s20, s12, s10
	s_addc_u32 s21, s13, s11
	global_load_dword v125, v94, s[20:21]
	s_add_u32 s20, s14, s10
	s_addc_u32 s21, s15, s11
	s_add_u32 s10, s16, s10
	s_addc_u32 s11, s17, s11
	global_load_dword v122, v94, s[20:21]
	global_load_dword v127, v94, s[10:11]
	s_add_i32 s20, s2, -1
	s_ashr_i32 s21, s20, 31
	s_lshl_b64 s[10:11], s[20:21], 2
	s_add_u32 s20, s12, s10
	s_addc_u32 s21, s13, s11
	global_load_dword v131, v94, s[20:21]
	s_add_u32 s20, s14, s10
	s_addc_u32 s21, s15, s11
	s_add_u32 s10, s16, s10
	s_addc_u32 s11, s17, s11
	s_ashr_i32 s3, s2, 31
	global_load_dword v124, v94, s[20:21]
	global_load_dword v150, v94, s[10:11]
	s_lshl_b64 s[10:11], s[2:3], 2
	s_add_u32 s20, s12, s10
	s_addc_u32 s21, s13, s11
	global_load_dword v151, v94, s[20:21]
	s_add_u32 s20, s14, s10
	s_addc_u32 s21, s15, s11
	global_load_dword v126, v94, s[20:21]
	s_add_u32 s10, s16, s10
	s_addc_u32 s11, s17, s11
	global_load_dword v154, v94, s[10:11]
	s_add_i32 s0, s0, s4
	s_add_i32 s2, s2, s1
	v_lshl_add_u64 v[78:79], v[68:69], 0, s[6:7]
	v_lshl_add_u64 v[80:81], v[70:71], 0, s[6:7]
	v_lshl_add_u64 v[82:83], v[72:73], 0, s[6:7]
	v_lshl_add_u64 v[84:85], v[74:75], 0, s[6:7]
	v_lshl_add_u64 v[56:57], v[56:57], 0, s[8:9]
	v_lshl_add_u64 v[58:59], v[58:59], 0, s[8:9]
	v_lshl_add_u64 v[60:61], v[60:61], 0, s[8:9]
	v_lshl_add_u64 v[62:63], v[62:63], 0, s[8:9]
	v_lshl_add_u64 v[64:65], v[64:65], 0, s[8:9]
	v_lshl_add_u64 v[66:67], v[66:67], 0, s[8:9]
	v_lshl_add_u64 v[68:69], v[68:69], 0, s[8:9]
	v_lshl_add_u64 v[70:71], v[70:71], 0, s[8:9]
	v_lshl_add_u64 v[72:73], v[72:73], 0, s[8:9]
	v_lshl_add_u64 v[74:75], v[74:75], 0, s[8:9]
	s_cmpk_lt_i32 s0, 0x2000
	s_waitcnt vmcnt(11)
	v_and_or_b32 v121, v121, 63, v86
	v_lshlrev_b32_e32 v121, 2, v121
	ds_bpermute_b32 v128, v121, v87
	s_waitcnt vmcnt(10)
	v_ashrrev_i32_e32 v121, 31, v120
	s_waitcnt vmcnt(9)
	v_mul_f32_e32 v130, 0x3d000000, v123
	s_waitcnt lgkmcnt(0)
	v_ashrrev_i32_e32 v129, 31, v128
	v_lshlrev_b64 v[120:121], 11, v[120:121]
	v_lshlrev_b64 v[128:129], 19, v[128:129]
	v_lshl_add_u64 v[120:121], v[128:129], 0, v[120:121]
	v_lshl_add_u64 v[132:133], v[40:41], 0, v[120:121]
	s_waitcnt vmcnt(8)
	v_and_or_b32 v123, v125, 63, v86
	v_lshlrev_b32_e32 v125, 2, v123
	ds_bpermute_b32 v128, v125, v87
	v_lshl_add_u64 v[134:135], v[42:43], 0, v[120:121]
	v_lshl_add_u64 v[136:137], v[44:45], 0, v[120:121]
	s_waitcnt vmcnt(7)
	v_ashrrev_i32_e32 v123, 31, v122
	v_lshl_add_u64 v[138:139], v[46:47], 0, v[120:121]
	v_lshl_add_u64 v[140:141], v[48:49], 0, v[120:121]
	v_lshl_add_u64 v[142:143], v[50:51], 0, v[120:121]
	v_lshl_add_u64 v[144:145], v[52:53], 0, v[120:121]
	v_lshl_add_u64 v[120:121], v[54:55], 0, v[120:121]
	global_load_dword v156, v[132:133], off
	global_load_dword v157, v[136:137], off
	s_waitcnt lgkmcnt(0)
	v_ashrrev_i32_e32 v129, 31, v128
	s_waitcnt vmcnt(7)
	v_and_or_b32 v125, v131, 63, v86
	v_lshlrev_b64 v[122:123], 11, v[122:123]
	global_load_dword v158, v[140:141], off
	global_load_dword v159, v[142:143], off
	global_load_dword v160, v[144:145], off
	s_nop 0
	global_load_dword v121, v[120:121], off
	v_mul_f32_e32 v120, 0x3d000000, v127
	v_lshlrev_b64 v[128:129], 19, v[128:129]
	v_lshlrev_b32_e32 v127, 2, v125
	v_lshl_add_u64 v[122:123], v[128:129], 0, v[122:123]
	ds_bpermute_b32 v128, v127, v87
	v_lshl_add_u64 v[132:133], v[40:41], 0, v[122:123]
	global_load_dword v131, v[132:133], off
	v_lshl_add_u64 v[136:137], v[42:43], 0, v[122:123]
	v_lshl_add_u64 v[140:141], v[44:45], 0, v[122:123]
	v_lshl_add_u64 v[142:143], v[46:47], 0, v[122:123]
	v_lshl_add_u64 v[144:145], v[48:49], 0, v[122:123]
	v_lshl_add_u64 v[146:147], v[50:51], 0, v[122:123]
	v_lshl_add_u64 v[148:149], v[52:53], 0, v[122:123]
	v_lshl_add_u64 v[122:123], v[54:55], 0, v[122:123]
	s_waitcnt vmcnt(11)
	v_ashrrev_i32_e32 v125, 31, v124
	global_load_dword v161, v[140:141], off
	global_load_dword v162, v[144:145], off
	global_load_dword v163, v[146:147], off
	global_load_dword v164, v[148:149], off
	s_nop 0
	global_load_dword v123, v[122:123], off
	s_waitcnt lgkmcnt(0)
	v_ashrrev_i32_e32 v129, 31, v128
	v_lshlrev_b64 v[124:125], 11, v[124:125]
	s_waitcnt vmcnt(14)
; __global__ void __launch_bounds__(NTHR, 2) fwd(Args args) {
;     ...
;             for (int k = 0; k < TOPK; ++k) { const int e = WSP(int, WS_SELE)[t * TOPK + k], p = WSP(int, WS_SELP)[t * TOPK + k]; gk[k] = WSP(float, WS_SELG)[t * TOPK + k] * Y8_INV;
;                 so[k] = ((size_t)__shfl(pb, e) * 256 + p) * D; }
;             f32x4 v[8]; float s = 0.f;
; #pragma unroll
;             for (int j = 0; j < 8; ++j) { const int cidx = (j * 64 + lane) * 4; f32x4 a = *(const f32x4*)(X2 + (size_t)t * D + cidx);
; #pragma unroll
;                 for (int k = 0; k < TOPK; ++k) { const unsigned y = *(const unsigned*)(YK + so[k] + cidx); const v2f lo = __builtin_amdgcn_cvt_pk_f32_fp8(y, false), hi = __builtin_amdgcn_cvt_pk_f32_fp8(y, true);
;                     a[0] += gk[k] * lo[0]; a[1] += gk[k] * lo[1]; a[2] += gk[k] * hi[0]; a[3] += gk[k] * hi[1]; }
;                 v[j] = a; s += (a[0] * a[0] + a[1] * a[1]) + (a[2] * a[2] + a[3] * a[3]); }
	v_and_or_b32 v127, v151, 63, v86
	v_lshlrev_b64 v[128:129], 19, v[128:129]
	v_lshlrev_b32_e32 v132, 2, v127
	v_lshl_add_u64 v[124:125], v[128:129], 0, v[124:125]
	ds_bpermute_b32 v128, v132, v87
	v_lshl_add_u64 v[132:133], v[40:41], 0, v[124:125]
	v_lshl_add_u64 v[144:145], v[44:45], 0, v[124:125]
	v_mul_f32_e32 v122, 0x3d000000, v150
	v_lshl_add_u64 v[140:141], v[42:43], 0, v[124:125]
	v_lshl_add_u64 v[146:147], v[46:47], 0, v[124:125]
	v_lshl_add_u64 v[148:149], v[48:49], 0, v[124:125]
	v_lshl_add_u64 v[150:151], v[50:51], 0, v[124:125]
	v_lshl_add_u64 v[152:153], v[52:53], 0, v[124:125]
	v_lshl_add_u64 v[124:125], v[54:55], 0, v[124:125]
	global_load_dword v133, v[132:133], off
	s_nop 0
	global_load_dword v165, v[144:145], off
	global_load_dword v166, v[148:149], off
	global_load_dword v167, v[150:151], off
	global_load_dword v168, v[152:153], off
	global_load_dword v169, v[124:125], off
	s_waitcnt vmcnt(19)
	v_ashrrev_i32_e32 v127, 31, v126
	s_waitcnt lgkmcnt(0)
	v_ashrrev_i32_e32 v129, 31, v128
	v_lshlrev_b64 v[126:127], 11, v[126:127]
	v_lshlrev_b64 v[124:125], 19, v[128:129]
	v_lshl_add_u64 v[124:125], v[124:125], 0, v[126:127]
	v_lshl_add_u64 v[126:127], v[40:41], 0, v[124:125]
	s_waitcnt vmcnt(18)
	v_mul_f32_e32 v132, 0x3d000000, v154
	v_lshl_add_u64 v[128:129], v[42:43], 0, v[124:125]
	v_lshl_add_u64 v[144:145], v[44:45], 0, v[124:125]
	v_lshl_add_u64 v[148:149], v[46:47], 0, v[124:125]
	v_lshl_add_u64 v[150:151], v[48:49], 0, v[124:125]
	v_lshl_add_u64 v[152:153], v[50:51], 0, v[124:125]
	v_lshl_add_u64 v[154:155], v[52:53], 0, v[124:125]
	v_lshl_add_u64 v[124:125], v[54:55], 0, v[124:125]
	global_load_dword v170, v[126:127], off
	global_load_dword v171, v[134:135], off
	global_load_dword v172, v[136:137], off
	global_load_dword v173, v[140:141], off
	global_load_dword v174, v[128:129], off
	global_load_dword v175, v[144:145], off
	global_load_dword v176, v[138:139], off
	global_load_dword v177, v[142:143], off
	global_load_dword v178, v[146:147], off
	global_load_dword v179, v[148:149], off
	global_load_dword v180, v[150:151], off
	global_load_dword v181, v[152:153], off
	global_load_dword v182, v[154:155], off
	global_load_dword v183, v[124:125], off
	s_waitcnt vmcnt(31)
	v_cvt_pk_f32_fp8_e32 v[124:125], v156
	s_waitcnt vmcnt(30)
	v_cvt_pk_f32_fp8_e32 v[128:129], v157
	v_cvt_pk_f32_fp8_sdwa v[134:135], v157 src0_sel:WORD_1
	s_waitcnt vmcnt(29)
	v_cvt_pk_f32_fp8_e32 v[136:137], v158
	v_cvt_pk_f32_fp8_sdwa v[138:139], v158 src0_sel:WORD_1
	s_waitcnt vmcnt(28)
	v_cvt_pk_f32_fp8_e32 v[140:141], v159
	v_cvt_pk_f32_fp8_sdwa v[142:143], v159 src0_sel:WORD_1
	v_cvt_pk_f32_fp8_sdwa v[126:127], v156 src0_sel:WORD_1
	s_waitcnt vmcnt(27)
	v_cvt_pk_f32_fp8_e32 v[144:145], v160
	v_cvt_pk_f32_fp8_sdwa v[146:147], v160 src0_sel:WORD_1
	s_waitcnt vmcnt(26)
	v_cvt_pk_f32_fp8_e32 v[148:149], v121
	v_cvt_pk_f32_fp8_sdwa v[150:151], v121 src0_sel:WORD_1
	s_waitcnt vmcnt(25)
	v_pk_fma_f32 v[116:117], v[128:129], v[130:131], v[116:117] op_sel_hi:[1,0,1]
	v_pk_fma_f32 v[118:119], v[130:131], v[134:135], v[118:119] op_sel_hi:[0,1,1]
	v_pk_fma_f32 v[96:97], v[136:137], v[130:131], v[96:97] op_sel_hi:[1,0,1]
	v_pk_fma_f32 v[98:99], v[130:131], v[138:139], v[98:99] op_sel_hi:[0,1,1]
	v_pk_fma_f32 v[100:101], v[140:141], v[130:131], v[100:101] op_sel_hi:[1,0,1]
	s_waitcnt vmcnt(24)
	v_cvt_pk_f32_fp8_e32 v[128:129], v161
	v_cvt_pk_f32_fp8_sdwa v[134:135], v161 src0_sel:WORD_1
	s_waitcnt vmcnt(23)
	v_cvt_pk_f32_fp8_e32 v[136:137], v162
	v_cvt_pk_f32_fp8_sdwa v[138:139], v162 src0_sel:WORD_1
	v_pk_fma_f32 v[102:103], v[130:131], v[142:143], v[102:103] op_sel_hi:[0,1,1]
	s_waitcnt vmcnt(22)
	v_cvt_pk_f32_fp8_e32 v[140:141], v163
	v_cvt_pk_f32_fp8_sdwa v[142:143], v163 src0_sel:WORD_1
	v_pk_fma_f32 v[112:113], v[124:125], v[130:131], v[112:113] op_sel_hi:[1,0,1]
	v_pk_fma_f32 v[114:115], v[130:131], v[126:127], v[114:115] op_sel_hi:[0,1,1]
	v_pk_fma_f32 v[104:105], v[144:145], v[130:131], v[104:105] op_sel_hi:[1,0,1]
	v_pk_fma_f32 v[106:107], v[130:131], v[146:147], v[106:107] op_sel_hi:[0,1,1]
	v_pk_fma_f32 v[108:109], v[148:149], v[130:131], v[108:109] op_sel_hi:[1,0,1]
	v_pk_fma_f32 v[110:111], v[130:131], v[150:151], v[110:111] op_sel_hi:[0,1,1]
	v_cvt_pk_f32_fp8_e32 v[124:125], v131
	v_cvt_pk_f32_fp8_sdwa v[126:127], v131 src0_sel:WORD_1
	s_waitcnt vmcnt(21)
	v_cvt_pk_f32_fp8_e32 v[144:145], v164
	v_cvt_pk_f32_fp8_sdwa v[146:147], v164 src0_sel:WORD_1
	s_waitcnt vmcnt(20)
	v_cvt_pk_f32_fp8_e32 v[148:149], v123
	v_cvt_pk_f32_fp8_sdwa v[150:151], v123 src0_sel:WORD_1
	v_pk_fma_f32 v[116:117], v[128:129], v[120:121], v[116:117] op_sel_hi:[1,0,1]
	v_pk_fma_f32 v[118:119], v[120:121], v[134:135], v[118:119] op_sel_hi:[0,1,1]
	s_waitcnt vmcnt(18)
	v_cvt_pk_f32_fp8_e32 v[128:129], v165
	v_cvt_pk_f32_fp8_sdwa v[134:135], v165 src0_sel:WORD_1
	v_pk_fma_f32 v[96:97], v[136:137], v[120:121], v[96:97] op_sel_hi:[1,0,1]
	v_pk_fma_f32 v[98:99], v[120:121], v[138:139], v[98:99] op_sel_hi:[0,1,1]
	s_waitcnt vmcnt(17)
	v_cvt_pk_f32_fp8_e32 v[136:137], v166
	v_cvt_pk_f32_fp8_sdwa v[138:139], v166 src0_sel:WORD_1
	v_pk_fma_f32 v[100:101], v[140:141], v[120:121], v[100:101] op_sel_hi:[1,0,1]
	v_pk_fma_f32 v[102:103], v[120:121], v[142:143], v[102:103] op_sel_hi:[0,1,1]
	s_waitcnt vmcnt(16)
	v_cvt_pk_f32_fp8_e32 v[140:141], v167
	v_cvt_pk_f32_fp8_sdwa v[142:143], v167 src0_sel:WORD_1
	v_pk_fma_f32 v[112:113], v[124:125], v[120:121], v[112:113] op_sel_hi:[1,0,1]
	v_pk_fma_f32 v[114:115], v[120:121], v[126:127], v[114:115] op_sel_hi:[0,1,1]
	v_pk_fma_f32 v[104:105], v[144:145], v[120:121], v[104:105] op_sel_hi:[1,0,1]
	v_pk_fma_f32 v[106:107], v[120:121], v[146:147], v[106:107] op_sel_hi:[0,1,1]
	v_pk_fma_f32 v[108:109], v[148:149], v[120:121], v[108:109] op_sel_hi:[1,0,1]
	v_pk_fma_f32 v[110:111], v[120:121], v[150:151], v[110:111] op_sel_hi:[0,1,1]
	v_cvt_pk_f32_fp8_e32 v[124:125], v133
	v_cvt_pk_f32_fp8_sdwa v[126:127], v133 src0_sel:WORD_1
	s_waitcnt vmcnt(15)
; __global__ void __launch_bounds__(NTHR, 2) fwd(Args args) {
;     ...
;             for (int j = 0; j < 8; ++j) { const int cidx = (j * 64 + lane) * 4; f32x4 a = *(const f32x4*)(X2 + (size_t)t * D + cidx);
; #pragma unroll
;                 for (int k = 0; k < TOPK; ++k) { const unsigned y = *(const unsigned*)(YK + so[k] + cidx); const v2f lo = __builtin_amdgcn_cvt_pk_f32_fp8(y, false), hi = __builtin_amdgcn_cvt_pk_f32_fp8(y, true);
;                     a[0] += gk[k] * lo[0]; a[1] += gk[k] * lo[1]; a[2] += gk[k] * hi[0]; a[3] += gk[k] * hi[1]; }
;                 v[j] = a; s += (a[0] * a[0] + a[1] * a[1]) + (a[2] * a[2] + a[3] * a[3]); }
;             const float r = rsqrtf(wave_sum(s) * (1.f / D) + EPS);
	v_cvt_pk_f32_fp8_e32 v[144:145], v168
	v_cvt_pk_f32_fp8_sdwa v[146:147], v168 src0_sel:WORD_1
	s_waitcnt vmcnt(14)
	v_cvt_pk_f32_fp8_e32 v[148:149], v169
	v_cvt_pk_f32_fp8_sdwa v[150:151], v169 src0_sel:WORD_1
	v_pk_fma_f32 v[116:117], v[128:129], v[122:123], v[116:117] op_sel_hi:[1,0,1]
	v_pk_fma_f32 v[118:119], v[122:123], v[134:135], v[118:119] op_sel_hi:[0,1,1]
	s_waitcnt vmcnt(12)
	v_cvt_pk_f32_fp8_e32 v[128:129], v171
	v_cvt_pk_f32_fp8_sdwa v[134:135], v171 src0_sel:WORD_1
	v_pk_fma_f32 v[96:97], v[136:137], v[122:123], v[96:97] op_sel_hi:[1,0,1]
	v_pk_fma_f32 v[98:99], v[122:123], v[138:139], v[98:99] op_sel_hi:[0,1,1]
	s_waitcnt vmcnt(11)
	v_cvt_pk_f32_fp8_e32 v[136:137], v172
	v_cvt_pk_f32_fp8_sdwa v[138:139], v172 src0_sel:WORD_1
	v_pk_fma_f32 v[100:101], v[140:141], v[122:123], v[100:101] op_sel_hi:[1,0,1]
	v_pk_fma_f32 v[102:103], v[122:123], v[142:143], v[102:103] op_sel_hi:[0,1,1]
	s_waitcnt vmcnt(10)
	v_cvt_pk_f32_fp8_e32 v[140:141], v173
	v_cvt_pk_f32_fp8_sdwa v[142:143], v173 src0_sel:WORD_1
	v_pk_fma_f32 v[112:113], v[124:125], v[122:123], v[112:113] op_sel_hi:[1,0,1]
	v_pk_fma_f32 v[114:115], v[122:123], v[126:127], v[114:115] op_sel_hi:[0,1,1]
	v_pk_fma_f32 v[104:105], v[144:145], v[122:123], v[104:105] op_sel_hi:[1,0,1]
	v_pk_fma_f32 v[106:107], v[122:123], v[146:147], v[106:107] op_sel_hi:[0,1,1]
	v_pk_fma_f32 v[108:109], v[148:149], v[122:123], v[108:109] op_sel_hi:[1,0,1]
	v_pk_fma_f32 v[110:111], v[122:123], v[150:151], v[110:111] op_sel_hi:[0,1,1]
	v_cvt_pk_f32_fp8_e32 v[124:125], v170
	v_cvt_pk_f32_fp8_sdwa v[126:127], v170 src0_sel:WORD_1
	s_waitcnt vmcnt(9)
	v_cvt_pk_f32_fp8_e32 v[144:145], v174
	v_cvt_pk_f32_fp8_sdwa v[146:147], v174 src0_sel:WORD_1
	s_waitcnt vmcnt(8)
	v_cvt_pk_f32_fp8_e32 v[148:149], v175
	v_cvt_pk_f32_fp8_sdwa v[150:151], v175 src0_sel:WORD_1
	s_waitcnt vmcnt(7)
	v_cvt_pk_f32_fp8_e32 v[152:153], v176
	v_cvt_pk_f32_fp8_sdwa v[154:155], v176 src0_sel:WORD_1
	s_waitcnt vmcnt(6)
	v_cvt_pk_f32_fp8_e32 v[156:157], v177
	v_cvt_pk_f32_fp8_sdwa v[158:159], v177 src0_sel:WORD_1
	v_pk_fma_f32 v[36:37], v[128:129], v[130:131], v[36:37] op_sel_hi:[1,0,1]
	v_pk_fma_f32 v[38:39], v[130:131], v[134:135], v[38:39] op_sel_hi:[0,1,1]
	s_waitcnt vmcnt(5)
	v_cvt_pk_f32_fp8_e32 v[160:161], v178
	v_cvt_pk_f32_fp8_sdwa v[162:163], v178 src0_sel:WORD_1
	v_pk_fma_f32 v[36:37], v[136:137], v[120:121], v[36:37] op_sel_hi:[1,0,1]
	v_pk_fma_f32 v[38:39], v[120:121], v[138:139], v[38:39] op_sel_hi:[0,1,1]
	s_waitcnt vmcnt(4)
	v_cvt_pk_f32_fp8_e32 v[164:165], v179
	v_cvt_pk_f32_fp8_sdwa v[166:167], v179 src0_sel:WORD_1
	v_pk_fma_f32 v[36:37], v[140:141], v[122:123], v[36:37] op_sel_hi:[1,0,1]
	v_pk_fma_f32 v[38:39], v[122:123], v[142:143], v[38:39] op_sel_hi:[0,1,1]
	s_waitcnt vmcnt(3)
	v_cvt_pk_f32_fp8_e32 v[168:169], v180
	v_cvt_pk_f32_fp8_sdwa v[170:171], v180 src0_sel:WORD_1
	s_waitcnt vmcnt(2)
	v_cvt_pk_f32_fp8_e32 v[172:173], v181
	v_cvt_pk_f32_fp8_sdwa v[174:175], v181 src0_sel:WORD_1
	s_waitcnt vmcnt(1)
	v_cvt_pk_f32_fp8_e32 v[176:177], v182
	v_cvt_pk_f32_fp8_sdwa v[178:179], v182 src0_sel:WORD_1
	s_waitcnt vmcnt(0)
	v_cvt_pk_f32_fp8_e32 v[180:181], v183
	v_cvt_pk_f32_fp8_sdwa v[182:183], v183 src0_sel:WORD_1
	v_pk_fma_f32 v[112:113], v[124:125], v[132:133], v[112:113] op_sel_hi:[1,0,1]
	v_pk_fma_f32 v[114:115], v[132:133], v[126:127], v[114:115] op_sel_hi:[0,1,1]
	v_pk_fma_f32 v[116:117], v[148:149], v[132:133], v[116:117] op_sel_hi:[1,0,1]
	v_pk_fma_f32 v[118:119], v[132:133], v[150:151], v[118:119] op_sel_hi:[0,1,1]
	v_pk_fma_f32 v[32:33], v[152:153], v[130:131], v[32:33] op_sel_hi:[1,0,1]
	v_pk_fma_f32 v[34:35], v[130:131], v[154:155], v[34:35] op_sel_hi:[0,1,1]
	v_pk_fma_f32 v[36:37], v[144:145], v[132:133], v[36:37] op_sel_hi:[1,0,1]
	v_pk_fma_f32 v[38:39], v[132:133], v[146:147], v[38:39] op_sel_hi:[0,1,1]
	v_mov_b32_e32 v126, v113
	v_mov_b32_e32 v130, v115
	v_mov_b32_e32 v136, v117
	v_mov_b32_e32 v137, v119
	v_pk_fma_f32 v[32:33], v[156:157], v[120:121], v[32:33] op_sel_hi:[1,0,1]
	v_pk_fma_f32 v[34:35], v[120:121], v[158:159], v[34:35] op_sel_hi:[0,1,1]
	v_mov_b32_e32 v127, v37
	v_mov_b32_e32 v131, v39
	v_mov_b32_e32 v124, v112
	v_mov_b32_e32 v128, v114
	v_mov_b32_e32 v134, v116
	v_mov_b32_e32 v135, v118
	v_pk_mul_f32 v[136:137], v[136:137], v[136:137]
	v_pk_fma_f32 v[32:33], v[160:161], v[122:123], v[32:33] op_sel_hi:[1,0,1]
	v_pk_fma_f32 v[34:35], v[122:123], v[162:163], v[34:35] op_sel_hi:[0,1,1]
	v_mov_b32_e32 v125, v36
	v_mov_b32_e32 v129, v38
	v_pk_mul_f32 v[126:127], v[126:127], v[126:127]
	v_pk_mul_f32 v[130:131], v[130:131], v[130:131]
	v_pk_fma_f32 v[134:135], v[134:135], v[134:135], v[136:137]
	v_pk_fma_f32 v[32:33], v[164:165], v[132:133], v[32:33] op_sel_hi:[1,0,1]
	v_pk_fma_f32 v[34:35], v[132:133], v[166:167], v[34:35] op_sel_hi:[0,1,1]
	v_pk_fma_f32 v[124:125], v[124:125], v[124:125], v[126:127]
	v_pk_fma_f32 v[126:127], v[128:129], v[128:129], v[130:131]
	v_pk_fma_f32 v[96:97], v[168:169], v[132:133], v[96:97] op_sel_hi:[1,0,1]
	v_pk_fma_f32 v[98:99], v[132:133], v[170:171], v[98:99] op_sel_hi:[0,1,1]
	v_pk_fma_f32 v[100:101], v[172:173], v[132:133], v[100:101] op_sel_hi:[1,0,1]
; __global__ void __launch_bounds__(NTHR, 2) fwd(Args args) {
;     ...
;                 v[j] = a; s += (a[0] * a[0] + a[1] * a[1]) + (a[2] * a[2] + a[3] * a[3]); }
;             const float r = rsqrtf(wave_sum(s) * (1.f / D) + EPS);
; #pragma unroll
;             for (int j = 0; j < 8; ++j) { const int cidx = (j * 64 + lane) * 4; *(f32x4*)(out + (size_t)t * D + cidx) = v[j] * r * fg[j]; }
	v_pk_fma_f32 v[102:103], v[132:133], v[174:175], v[102:103] op_sel_hi:[0,1,1]
	v_pk_fma_f32 v[104:105], v[176:177], v[132:133], v[104:105] op_sel_hi:[1,0,1]
	v_pk_fma_f32 v[106:107], v[132:133], v[178:179], v[106:107] op_sel_hi:[0,1,1]
	v_pk_fma_f32 v[108:109], v[180:181], v[132:133], v[108:109] op_sel_hi:[1,0,1]
	v_pk_fma_f32 v[110:111], v[132:133], v[182:183], v[110:111] op_sel_hi:[0,1,1]
	v_pk_add_f32 v[132:133], v[134:135], v[134:135] op_sel:[0,1] op_sel_hi:[1,0]
	v_mul_f32_e32 v134, v33, v33
	v_mul_f32_e32 v136, v35, v35
	v_pk_add_f32 v[124:125], v[124:125], v[126:127]
	v_pk_mul_f32 v[120:121], v[96:97], v[96:97]
	v_pk_mul_f32 v[138:139], v[98:99], v[98:99]
	v_pk_fma_f32 v[134:135], v[32:33], v[32:33], v[134:135] op_sel_hi:[1,1,0]
	v_pk_fma_f32 v[136:137], v[34:35], v[34:35], v[136:137] op_sel_hi:[1,1,0]
	v_pk_add_f32 v[124:125], v[124:125], v[124:125] op_sel:[0,1] op_sel_hi:[1,0]
	v_mov_b32_e32 v150, v101
	v_mov_b32_e32 v151, v103
	v_mov_b32_e32 v133, v121
	v_mov_b32_e32 v135, v138
	v_mov_b32_e32 v137, v139
	v_mov_b32_e32 v125, v120
	v_mov_b32_e32 v148, v100
	v_mov_b32_e32 v149, v102
	v_pk_mul_f32 v[122:123], v[150:151], v[150:151]
	v_pk_add_f32 v[126:127], v[134:135], v[136:137]
	v_pk_add_f32 v[120:121], v[124:125], v[132:133]
	v_mul_f32_e32 v152, v105, v105
	v_mul_f32_e32 v154, v107, v107
	v_pk_fma_f32 v[122:123], v[148:149], v[148:149], v[122:123]
	v_pk_add_f32 v[120:121], v[120:121], v[126:127]
	v_pk_mul_f32 v[156:157], v[108:109], v[108:109]
	v_pk_mul_f32 v[158:159], v[110:111], v[110:111]
	v_pk_fma_f32 v[140:141], v[104:105], v[104:105], v[152:153] op_sel_hi:[1,1,0]
	v_pk_fma_f32 v[142:143], v[106:107], v[106:107], v[154:155] op_sel_hi:[1,1,0]
	v_pk_add_f32 v[122:123], v[122:123], v[122:123] op_sel:[0,1] op_sel_hi:[1,0]
	v_pk_add_f32 v[120:121], v[120:121], v[120:121] op_sel:[0,1] op_sel_hi:[1,0]
	v_mov_b32_e32 v141, v158
	v_mov_b32_e32 v143, v159
	v_mov_b32_e32 v123, v157
	v_mov_b32_e32 v121, v156
	v_pk_add_f32 v[140:141], v[140:141], v[142:143]
	v_pk_add_f32 v[120:121], v[120:121], v[122:123]
	s_nop 0
	v_pk_add_f32 v[120:121], v[120:121], v[140:141]
	s_nop 0
	v_add_f32_e32 v120, v120, v121
	ds_bpermute_b32 v121, v88, v120
	s_waitcnt lgkmcnt(0)
	v_add_f32_e32 v120, v120, v121
	ds_bpermute_b32 v121, v89, v120
	s_waitcnt lgkmcnt(0)
	v_add_f32_e32 v120, v120, v121
	ds_bpermute_b32 v121, v90, v120
	s_waitcnt lgkmcnt(0)
	v_add_f32_e32 v120, v120, v121
	ds_bpermute_b32 v121, v91, v120
	s_waitcnt lgkmcnt(0)
	v_add_f32_e32 v120, v120, v121
	ds_bpermute_b32 v121, v92, v120
	s_waitcnt lgkmcnt(0)
	v_add_f32_e32 v120, v120, v121
	ds_bpermute_b32 v121, v93, v120
	s_waitcnt lgkmcnt(0)
	v_add_f32_e32 v120, v120, v121
	v_fmamk_f32 v120, v120, 0x3a000000, v95
	v_mul_f32_e32 v121, 0x4b800000, v120
	v_cmp_gt_f32_e32 vcc, s18, v120
	s_nop 1
	v_cndmask_b32_e32 v120, v120, v121, vcc
	v_rsq_f32_e32 v120, v120
	s_nop 0
	v_mul_f32_e32 v121, 0x45800000, v120
	v_cndmask_b32_e32 v120, v120, v121, vcc
	v_pk_mul_f32 v[112:113], v[120:121], v[112:113] op_sel_hi:[0,1]
	v_pk_mul_f32 v[114:115], v[120:121], v[114:115] op_sel_hi:[0,1]
	v_pk_mul_f32 v[36:37], v[120:121], v[36:37] op_sel_hi:[0,1]
	v_pk_mul_f32 v[38:39], v[120:121], v[38:39] op_sel_hi:[0,1]
	v_pk_mul_f32 v[116:117], v[120:121], v[116:117] op_sel_hi:[0,1]
	v_pk_mul_f32 v[118:119], v[120:121], v[118:119] op_sel_hi:[0,1]
	v_pk_mul_f32 v[122:123], v[120:121], v[32:33] op_sel_hi:[0,1]
	v_pk_mul_f32 v[124:125], v[120:121], v[34:35] op_sel_hi:[0,1]
	v_pk_mul_f32 v[126:127], v[120:121], v[96:97] op_sel_hi:[0,1]
	v_pk_mul_f32 v[128:129], v[120:121], v[98:99] op_sel_hi:[0,1]
	v_pk_mul_f32 v[130:131], v[120:121], v[100:101] op_sel_hi:[0,1]
	v_pk_mul_f32 v[132:133], v[120:121], v[102:103] op_sel_hi:[0,1]
	v_pk_mul_f32 v[134:135], v[120:121], v[104:105] op_sel_hi:[0,1]
	v_pk_mul_f32 v[136:137], v[120:121], v[106:107] op_sel_hi:[0,1]
	v_pk_mul_f32 v[138:139], v[120:121], v[108:109] op_sel_hi:[0,1]
	v_pk_mul_f32 v[120:121], v[120:121], v[110:111] op_sel_hi:[0,1]
	v_pk_mul_f32 v[34:35], v[114:115], v[2:3]
	v_pk_mul_f32 v[32:33], v[112:113], v[0:1]
	v_pk_mul_f32 v[38:39], v[38:39], v[6:7]
	v_pk_mul_f32 v[36:37], v[36:37], v[4:5]
	v_pk_mul_f32 v[98:99], v[118:119], v[10:11]
	v_pk_mul_f32 v[96:97], v[116:117], v[8:9]
	v_pk_mul_f32 v[102:103], v[124:125], v[14:15]
	v_pk_mul_f32 v[100:101], v[122:123], v[12:13]
	v_pk_mul_f32 v[106:107], v[128:129], v[18:19]
	v_pk_mul_f32 v[104:105], v[126:127], v[16:17]
	v_pk_mul_f32 v[110:111], v[132:133], v[22:23]
	v_pk_mul_f32 v[108:109], v[130:131], v[20:21]
	v_pk_mul_f32 v[114:115], v[136:137], v[26:27]
	v_pk_mul_f32 v[112:113], v[134:135], v[24:25]
	v_pk_mul_f32 v[118:119], v[120:121], v[30:31]
	v_pk_mul_f32 v[116:117], v[138:139], v[28:29]
	global_store_dwordx4 v[76:77], v[32:35], off nt
	global_store_dwordx4 v[76:77], v[36:39], off offset:1024 nt
	global_store_dwordx4 v[76:77], v[96:99], off offset:2048 nt
	global_store_dwordx4 v[76:77], v[100:103], off offset:3072 nt
	global_store_dwordx4 v[78:79], v[104:107], off nt
	global_store_dwordx4 v[80:81], v[108:111], off nt
	global_store_dwordx4 v[82:83], v[112:115], off nt
	global_store_dwordx4 v[84:85], v[116:119], off nt
	s_cbranch_scc1 .LBB0_1674
